# attention ride: x512 folded into v_cvt_scalef32_pk_fp8_f32 (scale 2^-9), clamp on the unscaled value: 8 fewer VALU per step
# baseline (speedup 1.0000x reference)
; DI int v_st(int k, int c) { const int kk = (k & ~0xC) | ((k & 4) << 1) | ((k & 8) >> 1); return ((kk >> 3) * 4 + (c >> 5)) * 512 + ((kk & 7) * 32 + (c & 31)) * 2; }
; DI void attn_pass(const Frame& F, CvRide& cv, const bf16_t* __restrict__ Qb, const bf16_t* __restrict__ Kh, const bf16_t* __restrict__ Vh, char* lds, f32x16 (&o)[4], float& l_out, const int wave_s) {
;     ...
;     float m_ref = 0.f, l_reg = 0.f; bf16x8 qr[4]; f32x16 negm = f32x16{};
; #pragma unroll
;     for (int d = 0; d < 4; ++d) o[d] = f32x16{};
;     const bf16_t* Qw = Qb + (size_t)(wid * 32 + r32) * 64 + hi * 8;
; #pragma unroll
;     for (int d0 = 0; d0 < 4; ++d0) qr[d0] = *reinterpret_cast<const bf16x8*>(Qw + d0 * 16);
;     const int sr = tid >> 4, sc = (tid & 15) * 8, vst0 = v_st(sr, sc), vst1 = v_st(32 + sr, sc);
;     const int kr = tid >> 3, kcb = (tid & 7) * 16, kst = AT_KSWZ(kr, kcb);
;     const int vb0 = (int)(uintptr_t)V_lds + v_rd_base(lane);
;     struct { bf16x8 vs0, vs1, ks0; } sr_[1];
;     const unsigned gvo = (unsigned)((sr * 128 + sc) * 2), gko = (unsigned)((kr * 64 + (tid & 7) * 8) * 2);
;     ...
;     const unsigned cv_ldo = (unsigned)(((tid >> 4) * 2 * 2048 + (tid & 15) * 4) * 4), cv_sto = (unsigned)((tid >> 3) * 2048 + 8 * (tid & 7));
;     const int cv_lw = OFF_CV + (4 * (tid & 15)) * 68 + 2 * (tid >> 4), cv_lr = OFF_CV + (tid >> 3) * 68 + 8 * (tid & 7);
;     f32x4 cvA = f32x4{}, cvB = f32x4{}; unsigned cvr0 = 0, cvr1 = 0;
;     ...
;     f32x16 pA0, pA1, pB0, pB1; float alA, alB; bf16x8 pa0, pa1, pa2, pa3; constexpr int NT = S / 64;
;     constexpr int SE = 0;
;     {
;         bf16x8 v10 = *reinterpret_cast<const bf16x8*>(&Vh[(size_t)(64 + sr) * 128 + sc]), v11 = *reinterpret_cast<const bf16x8*>(&Vh[(size_t)(96 + sr) * 128 + sc]);
;         bf16x8 k10 = *reinterpret_cast<const bf16x8*>(&Kh[(size_t)(64 + kr) * 64 + (tid & 7) * 8]);
;         AT_SLOAD(SE, 0); asm volatile("s_waitcnt vmcnt(0)" ::: "memory");
;         __syncthreads();
;         AT_SWRITE(0, SE);
;         *(bf16x8*)(V_lds + SHM_V + vst0) = v10; *(bf16x8*)(V_lds + SHM_V + vst1) = v11; *(bf16x8*)(K_lds + SHM_K + kst) = k10;
;         __syncthreads();
;     }
;     qkt(pA0, pA1, K_lds, qr, negm, r32, hi); partialSM(pA0, pA1, m_ref, negm, alA);
;     int s_prev = 0, s_cur = 1, s_next = 2;
.LBB4_691:
	v_lshlrev_b32_e32 v24, 4, v21
	v_lshlrev_b32_e32 v23, 3, v21
	v_and_b32_e32 v24, 0xc0, v24
	v_lshlrev_b32_e32 v21, 1, v21
	v_and_or_b32 v24, v23, 24, v24
	v_and_b32_e32 v21, 32, v21
	v_and_b32_e32 v23, 0x100, v23
	s_cmp_lg_u32 0, -1
	v_or3_b32 v199, v24, v21, v23
	s_cselect_b32 s2, 0, 0
	v_add_u32_e32 v192, s2, v199
	s_movk_i32 s2, 0x44
	v_lshl_or_b32 v209, v16, 14, v18
	v_mul_lo_u32 v16, v20, s2
	v_exp_f32_e32 v216, v0
	v_exp_f32_e32 v218, v1
	v_exp_f32_e32 v179, v2
	v_exp_f32_e32 v217, v3
	v_exp_f32_e32 v177, v4
	v_exp_f32_e32 v215, v5
	v_exp_f32_e32 v176, v6
	v_exp_f32_e32 v178, v7
	v_exp_f32_e32 v173, v8
	v_exp_f32_e32 v175, v9
	v_exp_f32_e32 v171, v10
	v_exp_f32_e32 v174, v11
	v_exp_f32_e32 v169, v12
	v_exp_f32_e32 v172, v13
	v_exp_f32_e32 v168, v14
	v_exp_f32_e32 v170, v15
	v_add_u32_e32 v0, 0, v19
	s_mov_b32 s2, 0x22000
	v_mov_b32_e32 v182, 0
	v_add3_u32 v190, v0, v16, s2
	v_add_u32_e32 v0, 0, v22
	v_mov_b32_e32 v162, v182
	v_mov_b32_e32 v163, v182
	v_mov_b32_e32 v32, v182
	v_mov_b32_e32 v33, v182
	v_mov_b32_e32 v46, v182
	v_mov_b32_e32 v47, v182
	v_lshl_or_b32 v189, v20, 11, v19
	v_add3_u32 v191, v0, v17, s2
	v_mov_b32_e32 v183, v182
	v_mov_b32_e32 v160, v182
	v_mov_b32_e32 v161, v182
	v_mov_b32_e32 v34, v182
	v_mov_b32_e32 v35, v182
	v_mov_b32_e32 v36, v182
	v_mov_b32_e32 v37, v182
	v_mov_b32_e32 v38, v182
	v_mov_b32_e32 v39, v182
	v_mov_b32_e32 v40, v182
	v_mov_b32_e32 v41, v182
	v_mov_b32_e32 v42, v182
	v_mov_b32_e32 v43, v182
	v_mov_b32_e32 v44, v182
	v_mov_b32_e32 v45, v182
	v_mov_b64_e32 v[62:63], v[46:47]
	v_mov_b64_e32 v[16:17], v[32:33]
	v_mov_b64_e32 v[0:1], v[32:33]
	v_mov_b64_e32 v[166:167], v[162:163]
	s_mov_b32 s36, -1
	s_mul_i32 s59, s33, 6
	s_mov_b32 s64, 2
	s_mov_b64 s[12:13], 0
	s_mov_b32 s62, 0xc3e00000
	v_mov_b32_e32 v211, 0x43e00000
	s_mov_b64 s[28:29], s[16:17]
	s_mov_b64 s[30:31], s[18:19]
	s_mov_b32 s58, 0
	s_mov_b32 s26, 0
	s_mov_b64 s[10:11], 0
	s_mov_b64 s[8:9], 0
	v_mov_b64_e32 v[60:61], v[44:45]
	v_mov_b64_e32 v[58:59], v[42:43]
	v_mov_b64_e32 v[56:57], v[40:41]
	v_mov_b64_e32 v[54:55], v[38:39]
	v_mov_b64_e32 v[52:53], v[36:37]
	v_mov_b64_e32 v[50:51], v[34:35]
	v_mov_b64_e32 v[48:49], v[32:33]
	v_mov_b64_e32 v[18:19], v[34:35]
	v_mov_b64_e32 v[20:21], v[36:37]
	v_mov_b64_e32 v[22:23], v[38:39]
	v_mov_b64_e32 v[24:25], v[40:41]
	v_mov_b64_e32 v[26:27], v[42:43]
	v_mov_b64_e32 v[28:29], v[44:45]
	v_mov_b64_e32 v[30:31], v[46:47]
	v_mov_b64_e32 v[2:3], v[34:35]
	v_mov_b64_e32 v[4:5], v[36:37]
	v_mov_b64_e32 v[6:7], v[38:39]
	v_mov_b64_e32 v[8:9], v[40:41]
	v_mov_b64_e32 v[10:11], v[42:43]
	v_mov_b64_e32 v[12:13], v[44:45]
	v_mov_b64_e32 v[14:15], v[46:47]
	v_mov_b64_e32 v[164:165], v[160:161]
	s_mov_b32 s34, 0
	s_mov_b32 s65, 1
	v_mov_b64_e32 v[184:185], v[182:183]
	v_mov_b32_e32 v81, v80
	v_mov_b32_e32 v82, v80
	v_mov_b32_e32 v83, v80
	v_mov_b32_e32 v84, v80
	v_mov_b32_e32 v85, v80
	v_mov_b32_e32 v86, v80
	v_mov_b32_e32 v87, v80
	v_mov_b32_e32 v88, v80
	v_mov_b32_e32 v89, v80
	v_mov_b32_e32 v90, v80
	v_mov_b32_e32 v91, v80
	v_mov_b32_e32 v92, v80
	v_mov_b32_e32 v93, v80
	v_mov_b32_e32 v94, v80
	v_mov_b32_e32 v95, v80
	v_mov_b32_e32 v255, 0x3f600000
	s_mov_b32 s93, 0x3b000000

; #define AT_SBAR() __builtin_amdgcn_sched_barrier(0)
; template <int OFF> DI s16x4 tr_read(int vb) { s16x4 r; asm volatile("ds_read_b64_tr_b16 %0, %1 offset:%2" : "=&v"(r) : "v"(vb), "i"(OFF) : "memory"); return r; }
; template <int D0> DI void pv_one(f32x16& od, int vb, bf16x8 pa0, bf16x8 pa1, bf16x8 pa2, bf16x8 pa3) {
;     const s16x4 l0 = tr_read<v_rd_off(D0, 0, 0)>(vb), h0 = tr_read<v_rd_off(D0, 0, 1)>(vb), l1 = tr_read<v_rd_off(D0, 1, 0)>(vb), h1 = tr_read<v_rd_off(D0, 1, 1)>(vb);
;     const s16x4 l2 = tr_read<v_rd_off(D0, 2, 0)>(vb), h2 = tr_read<v_rd_off(D0, 2, 1)>(vb), l3 = tr_read<v_rd_off(D0, 3, 0)>(vb), h3 = tr_read<v_rd_off(D0, 3, 1)>(vb);
;     asm volatile("s_waitcnt lgkmcnt(0)" ::: "memory"); AT_SBAR();
;     ...
;     od = __builtin_amdgcn_mfma_f32_32x32x16_bf16(AT_PK(l0, h0), pa0, od, 0, 0, 0);
;     od = __builtin_amdgcn_mfma_f32_32x32x16_bf16(AT_PK(l1, h1), pa1, od, 0, 0, 0);
;     od = __builtin_amdgcn_mfma_f32_32x32x16_bf16(AT_PK(l2, h2), pa2, od, 0, 0, 0);
;     od = __builtin_amdgcn_mfma_f32_32x32x16_bf16(AT_PK(l3, h3), pa3, od, 0, 0, 0);
; DI void attn_pass(const Frame& F, CvRide& cv, const bf16_t* __restrict__ Qb, const bf16_t* __restrict__ Kh, const bf16_t* __restrict__ Vh, char* lds, f32x16 (&o)[4], float& l_out, const int wave_s) {
;     ...
;     const unsigned cv_ldo = (unsigned)(((tid >> 4) * 2 * 2048 + (tid & 15) * 4) * 4), cv_sto = (unsigned)((tid >> 3) * 2048 + 8 * (tid & 7));
;     const int cv_lw = OFF_CV + (4 * (tid & 15)) * 68 + 2 * (tid >> 4), cv_lr = OFF_CV + (tid >> 3) * 68 + 8 * (tid & 7);
;     f32x4 cvA = f32x4{}, cvB = f32x4{}; unsigned cvr0 = 0, cvr1 = 0;
.LBB4_706:
	ds_read_b64_tr_b16 v[214:215], v186 offset:0x600
	ds_read_b64_tr_b16 v[216:217], v186 offset:0xe00
	ds_read_b64_tr_b16 v[218:219], v186 offset:0x1600
	ds_read_b64_tr_b16 v[220:221], v186 offset:0x1e00
	ds_read_b64_tr_b16 v[222:223], v186 offset:0x2600
	ds_read_b64_tr_b16 v[224:225], v186 offset:0x2e00
	ds_read_b64_tr_b16 v[226:227], v186 offset:0x3600
	ds_read_b64_tr_b16 v[228:229], v186 offset:0x3e00
	s_waitcnt lgkmcnt(0)
	s_nop 0
	v_mfma_f32_32x32x16_bf16 v[0:15], v[214:217], v[96:99], v[0:15]
	s_lshl_b32 s2, s64, 14
	s_add_i32 s2, s2, 0
	s_lshl_b32 s3, s64, 13
	v_add_u32_e32 v96, s2, v200
	s_sub_i32 s78, s2, s3
	s_waitcnt vmcnt(0)
	v_add_u32_e32 v97, s2, v201
	v_mfma_f32_32x32x16_bf16 v[0:15], v[218:221], v[108:111], v[0:15]
	ds_write_b128 v96, v[176:179]
	v_add_u32_e32 v96, s78, v202
	ds_write_b128 v97, v[172:175]
	ds_write_b128 v96, v[168:171] offset:49152
	s_andn2_b64 s[2:3], exec, s[34:35]
	s_andn2_b64 vcc, exec, s[34:35]
	v_mfma_f32_32x32x16_bf16 v[0:15], v[222:225], v[100:103], v[0:15]
	v_mfma_f32_32x32x16_bf16 v[0:15], v[226:229], v[104:107], v[0:15]
	s_cbranch_vccnz .LBB4_711
	v_med3_f32 v97, v160, -v255, v255
	v_med3_f32 v98, v164, -v255, v255
	v_cvt_scalef32_pk_fp8_f32 v99, v97, v98, s93
	v_med3_f32 v97, v161, -v255, v255
	v_med3_f32 v98, v165, -v255, v255
	v_cvt_scalef32_pk_fp8_f32 v100, v97, v98, s93
	v_med3_f32 v97, v162, -v255, v255
	v_med3_f32 v98, v166, -v255, v255
	s_bitcmp1_b32 s58, 0
	v_cvt_scalef32_pk_fp8_f32 v101, v97, v98, s93
	s_cselect_b32 s8, 0x1100, 0
	v_med3_f32 v97, v163, -v255, v255
	v_med3_f32 v98, v167, -v255, v255
	v_cmp_eq_u32_e32 vcc, 0, v181
	v_add_u32_e32 v96, s8, v191
	v_cvt_scalef32_pk_fp8_f32 v102, v97, v98, s93
	s_and_b64 vcc, exec, vcc
	s_and_b32 s34, s58, 31
	ds_write_b16 v96, v99
	ds_write_b16 v96, v100 offset:68
	ds_write_b16 v96, v101 offset:136
	ds_write_b16 v96, v102 offset:204
	s_cbranch_vccnz .LBB4_735
	s_lshl_b32 s8, s34, 7
	s_lshl_b32 s9, s58, 6
	s_and_b32 s8, s8, 0xf00
	s_and_b32 s9, s9, 64
	s_or_b32 s26, s8, s9
	s_cbranch_execnz .LBB4_710

; #define AT_SBAR() __builtin_amdgcn_sched_barrier(0)
; template <int OFF> DI s16x4 tr_read(int vb) { s16x4 r; asm volatile("ds_read_b64_tr_b16 %0, %1 offset:%2" : "=&v"(r) : "v"(vb), "i"(OFF) : "memory"); return r; }
; template <int D0> DI void pv_one(f32x16& od, int vb, bf16x8 pa0, bf16x8 pa1, bf16x8 pa2, bf16x8 pa3) {
;     const s16x4 l0 = tr_read<v_rd_off(D0, 0, 0)>(vb), h0 = tr_read<v_rd_off(D0, 0, 1)>(vb), l1 = tr_read<v_rd_off(D0, 1, 0)>(vb), h1 = tr_read<v_rd_off(D0, 1, 1)>(vb);
;     const s16x4 l2 = tr_read<v_rd_off(D0, 2, 0)>(vb), h2 = tr_read<v_rd_off(D0, 2, 1)>(vb), l3 = tr_read<v_rd_off(D0, 3, 0)>(vb), h3 = tr_read<v_rd_off(D0, 3, 1)>(vb);
;     asm volatile("s_waitcnt lgkmcnt(0)" ::: "memory"); AT_SBAR();
;     ...
;     od = __builtin_amdgcn_mfma_f32_32x32x16_bf16(AT_PK(l0, h0), pa0, od, 0, 0, 0);
;     od = __builtin_amdgcn_mfma_f32_32x32x16_bf16(AT_PK(l1, h1), pa1, od, 0, 0, 0);
;     od = __builtin_amdgcn_mfma_f32_32x32x16_bf16(AT_PK(l2, h2), pa2, od, 0, 0, 0);
;     od = __builtin_amdgcn_mfma_f32_32x32x16_bf16(AT_PK(l3, h3), pa3, od, 0, 0, 0);
; DI void attn_pass(const Frame& F, CvRide& cv, const bf16_t* __restrict__ Qb, const bf16_t* __restrict__ Kh, const bf16_t* __restrict__ Vh, char* lds, f32x16 (&o)[4], float& l_out, const int wave_s) {
;     ...
;     const unsigned cv_ldo = (unsigned)(((tid >> 4) * 2 * 2048 + (tid & 15) * 4) * 4), cv_sto = (unsigned)((tid >> 3) * 2048 + 8 * (tid & 7));
;     const int cv_lw = OFF_CV + (4 * (tid & 15)) * 68 + 2 * (tid >> 4), cv_lr = OFF_CV + (tid >> 3) * 68 + 8 * (tid & 7);
;     f32x4 cvA = f32x4{}, cvB = f32x4{}; unsigned cvr0 = 0, cvr1 = 0;
.LBB4_726:
	ds_read_b64_tr_b16 v[216:217], v215 offset:0x600
	ds_read_b64_tr_b16 v[218:219], v215 offset:0xe00
	ds_read_b64_tr_b16 v[220:221], v215 offset:0x1600
	ds_read_b64_tr_b16 v[222:223], v215 offset:0x1e00
	ds_read_b64_tr_b16 v[224:225], v215 offset:0x2600
	ds_read_b64_tr_b16 v[226:227], v215 offset:0x2e00
	ds_read_b64_tr_b16 v[228:229], v215 offset:0x3600
	ds_read_b64_tr_b16 v[230:231], v215 offset:0x3e00
	s_waitcnt lgkmcnt(0)
	s_nop 0
	v_mfma_f32_32x32x16_bf16 v[0:15], v[216:219], v[120:123], v[0:15]
	s_add_i32 s2, s67, 0
	v_add_u32_e32 v120, s2, v200
	s_waitcnt vmcnt(0)
	ds_write_b128 v120, v[176:179]
	s_mov_b32 s26, 0
	s_andn2_b64 vcc, exec, s[34:35]
	v_mfma_f32_32x32x16_bf16 v[0:15], v[220:223], v[124:127], v[0:15]
	v_mfma_f32_32x32x16_bf16 v[0:15], v[224:227], v[112:115], v[0:15]
	v_add_u32_e32 v112, s2, v201
	ds_write_b128 v112, v[172:175]
	v_lshl_add_u32 v112, s65, 13, v203
	ds_write_b128 v112, v[168:171] offset:49152
	s_andn2_b64 s[2:3], exec, s[34:35]
	v_mfma_f32_32x32x16_bf16 v[0:15], v[228:231], v[116:119], v[0:15]
	s_cbranch_vccnz .LBB4_731
	v_med3_f32 v113, v160, -v255, v255
	v_med3_f32 v114, v164, -v255, v255
	v_cvt_scalef32_pk_fp8_f32 v115, v113, v114, s93
	v_med3_f32 v113, v161, -v255, v255
	v_med3_f32 v114, v165, -v255, v255
	v_cvt_scalef32_pk_fp8_f32 v116, v113, v114, s93
	v_med3_f32 v113, v162, -v255, v255
	v_med3_f32 v114, v166, -v255, v255
	s_bitcmp1_b32 s58, 0
	v_cvt_scalef32_pk_fp8_f32 v117, v113, v114, s93
	s_cselect_b32 s8, 0x1100, 0
	v_med3_f32 v113, v163, -v255, v255
	v_med3_f32 v114, v167, -v255, v255
	v_cmp_eq_u32_e32 vcc, 0, v181
	v_add_u32_e32 v112, s8, v191
	v_cvt_scalef32_pk_fp8_f32 v118, v113, v114, s93
	s_and_b64 vcc, exec, vcc
	s_and_b32 s37, s58, 31
	ds_write_b16 v112, v115
	ds_write_b16 v112, v116 offset:68
	ds_write_b16 v112, v117 offset:136
	ds_write_b16 v112, v118 offset:204
	s_cbranch_vccnz .LBB4_736
	s_lshl_b32 s8, s37, 7
	s_lshl_b32 s9, s58, 6
	s_and_b32 s8, s8, 0xf00
	s_and_b32 s9, s9, 64
	s_or_b32 s26, s8, s9
	s_cbranch_execnz .LBB4_730

; DI int v_st(int k, int c) { const int kk = (k & ~0xC) | ((k & 4) << 1) | ((k & 8) >> 1); return ((kk >> 3) * 4 + (c >> 5)) * 512 + ((kk & 7) * 32 + (c & 31)) * 2; }
; DI void attn_pass(const Frame& F, CvRide& cv, const bf16_t* __restrict__ Qb, const bf16_t* __restrict__ Kh, const bf16_t* __restrict__ Vh, char* lds, f32x16 (&o)[4], float& l_out, const int wave_s) {
;     ...
;     float m_ref = 0.f, l_reg = 0.f; bf16x8 qr[4]; f32x16 negm = f32x16{};
; #pragma unroll
;     for (int d = 0; d < 4; ++d) o[d] = f32x16{};
;     const bf16_t* Qw = Qb + (size_t)(wid * 32 + r32) * 64 + hi * 8;
; #pragma unroll
;     for (int d0 = 0; d0 < 4; ++d0) qr[d0] = *reinterpret_cast<const bf16x8*>(Qw + d0 * 16);
;     const int sr = tid >> 4, sc = (tid & 15) * 8, vst0 = v_st(sr, sc), vst1 = v_st(32 + sr, sc);
;     const int kr = tid >> 3, kcb = (tid & 7) * 16, kst = AT_KSWZ(kr, kcb);
;     const int vb0 = (int)(uintptr_t)V_lds + v_rd_base(lane);
;     struct { bf16x8 vs0, vs1, ks0; } sr_[1];
;     const unsigned gvo = (unsigned)((sr * 128 + sc) * 2), gko = (unsigned)((kr * 64 + (tid & 7) * 8) * 2);
;     ...
;     const unsigned cv_ldo = (unsigned)(((tid >> 4) * 2 * 2048 + (tid & 15) * 4) * 4), cv_sto = (unsigned)((tid >> 3) * 2048 + 8 * (tid & 7));
;     const int cv_lw = OFF_CV + (4 * (tid & 15)) * 68 + 2 * (tid >> 4), cv_lr = OFF_CV + (tid >> 3) * 68 + 8 * (tid & 7);
;     f32x4 cvA = f32x4{}, cvB = f32x4{}; unsigned cvr0 = 0, cvr1 = 0;
;     ...
;     f32x16 pA0, pA1, pB0, pB1; float alA, alB; bf16x8 pa0, pa1, pa2, pa3; constexpr int NT = S / 64;
;     constexpr int SE = 0;
;     {
;         bf16x8 v10 = *reinterpret_cast<const bf16x8*>(&Vh[(size_t)(64 + sr) * 128 + sc]), v11 = *reinterpret_cast<const bf16x8*>(&Vh[(size_t)(96 + sr) * 128 + sc]);
;         bf16x8 k10 = *reinterpret_cast<const bf16x8*>(&Kh[(size_t)(64 + kr) * 64 + (tid & 7) * 8]);
;         AT_SLOAD(SE, 0); asm volatile("s_waitcnt vmcnt(0)" ::: "memory");
;         __syncthreads();
;         AT_SWRITE(0, SE);
;         *(bf16x8*)(V_lds + SHM_V + vst0) = v10; *(bf16x8*)(V_lds + SHM_V + vst1) = v11; *(bf16x8*)(K_lds + SHM_K + kst) = k10;
;         __syncthreads();
;     }
;     qkt(pA0, pA1, K_lds, qr, negm, r32, hi); partialSM(pA0, pA1, m_ref, negm, alA);
;     int s_prev = 0, s_cur = 1, s_next = 2;
.LBB4_764:
	v_lshlrev_b32_e32 v24, 4, v22
	v_lshlrev_b32_e32 v23, 3, v22
	v_and_b32_e32 v24, 0xc0, v24
	v_lshlrev_b32_e32 v22, 1, v22
	v_and_or_b32 v24, v23, 24, v24
	v_and_b32_e32 v22, 32, v22
	v_and_b32_e32 v23, 0x100, v23
	s_cmp_lg_u32 0, -1
	v_or3_b32 v202, v24, v22, v23
	s_cselect_b32 s2, 0, 0
	v_add_u32_e32 v192, s2, v202
	s_movk_i32 s2, 0x44
	v_lshl_or_b32 v213, v16, 14, v18
	v_mul_lo_u32 v16, v20, s2
	v_exp_f32_e32 v220, v0
	v_exp_f32_e32 v222, v1
	v_exp_f32_e32 v179, v2
	v_exp_f32_e32 v221, v3
	v_exp_f32_e32 v177, v4
	v_exp_f32_e32 v219, v5
	v_exp_f32_e32 v176, v6
	v_exp_f32_e32 v178, v7
	v_exp_f32_e32 v173, v8
	v_exp_f32_e32 v175, v9
	v_exp_f32_e32 v171, v10
	v_exp_f32_e32 v174, v11
	v_exp_f32_e32 v169, v12
	v_exp_f32_e32 v172, v13
	v_exp_f32_e32 v168, v14
	v_exp_f32_e32 v170, v15
	v_add_u32_e32 v0, 0, v21
	s_mov_b32 s2, 0x22000
	v_add3_u32 v194, v0, v16, s2
	v_add_u32_e32 v0, 0, v19
	v_mov_b32_e32 v162, v183
	v_mov_b32_e32 v163, v183
	v_mov_b32_e32 v48, v183
	v_mov_b32_e32 v49, v183
	v_lshl_or_b32 v193, v20, 11, v21
	v_add3_u32 v195, v0, v17, s2
	v_mov_b32_e32 v182, v183
	v_mov_b32_e32 v160, v183
	v_mov_b32_e32 v161, v183
	v_mov_b32_e32 v50, v183
	v_mov_b32_e32 v51, v183
	v_mov_b32_e32 v52, v183
	v_mov_b32_e32 v53, v183
	v_mov_b32_e32 v54, v183
	v_mov_b32_e32 v55, v183
	v_mov_b32_e32 v56, v183
	v_mov_b32_e32 v57, v183
	v_mov_b32_e32 v58, v183
	v_mov_b32_e32 v59, v183
	v_mov_b32_e32 v60, v183
	v_mov_b32_e32 v61, v183
	v_mov_b32_e32 v62, v183
	v_mov_b32_e32 v63, v183
	v_mov_b64_e32 v[32:33], v[48:49]
	v_mov_b64_e32 v[16:17], v[48:49]
	v_mov_b64_e32 v[0:1], v[48:49]
	v_mov_b64_e32 v[166:167], v[162:163]
	s_mov_b32 s27, 1
	s_mov_b32 s28, 0xc3e00000
	v_mov_b32_e32 v214, 0x43e00000
	s_mov_b32 s20, 0
	v_mov_b64_e32 v[34:35], v[50:51]
	v_mov_b64_e32 v[36:37], v[52:53]
	v_mov_b64_e32 v[38:39], v[54:55]
	v_mov_b64_e32 v[40:41], v[56:57]
	v_mov_b64_e32 v[42:43], v[58:59]
	v_mov_b64_e32 v[44:45], v[60:61]
	v_mov_b64_e32 v[46:47], v[62:63]
	v_mov_b64_e32 v[18:19], v[50:51]
	v_mov_b64_e32 v[20:21], v[52:53]
	v_mov_b64_e32 v[22:23], v[54:55]
	v_mov_b64_e32 v[24:25], v[56:57]
	v_mov_b64_e32 v[26:27], v[58:59]
	v_mov_b64_e32 v[28:29], v[60:61]
	v_mov_b64_e32 v[30:31], v[62:63]
	v_mov_b64_e32 v[2:3], v[50:51]
	v_mov_b64_e32 v[4:5], v[52:53]
	v_mov_b64_e32 v[6:7], v[54:55]
	v_mov_b64_e32 v[8:9], v[56:57]
	v_mov_b64_e32 v[10:11], v[58:59]
	v_mov_b64_e32 v[12:13], v[60:61]
	v_mov_b64_e32 v[14:15], v[62:63]
	v_mov_b64_e32 v[164:165], v[160:161]
	s_mov_b32 s22, 0
	s_mov_b32 s29, 1
	v_mov_b64_e32 v[184:185], v[182:183]
	v_mov_b32_e32 v81, v80
	v_mov_b32_e32 v82, v80
	v_mov_b32_e32 v83, v80
	v_mov_b32_e32 v84, v80
	v_mov_b32_e32 v85, v80
	v_mov_b32_e32 v86, v80
	v_mov_b32_e32 v87, v80
	v_mov_b32_e32 v88, v80
	v_mov_b32_e32 v89, v80
	v_mov_b32_e32 v90, v80
	v_mov_b32_e32 v91, v80
	v_mov_b32_e32 v92, v80
	v_mov_b32_e32 v93, v80
	v_mov_b32_e32 v94, v80
	v_mov_b32_e32 v95, v80
	v_mov_b32_e32 v255, 0x3f600000
	s_mov_b32 s93, 0x3b000000

; #define AT_SBAR() __builtin_amdgcn_sched_barrier(0)
; template <int OFF> DI s16x4 tr_read(int vb) { s16x4 r; asm volatile("ds_read_b64_tr_b16 %0, %1 offset:%2" : "=&v"(r) : "v"(vb), "i"(OFF) : "memory"); return r; }
; template <int D0> DI void pv_one(f32x16& od, int vb, bf16x8 pa0, bf16x8 pa1, bf16x8 pa2, bf16x8 pa3) {
;     const s16x4 l0 = tr_read<v_rd_off(D0, 0, 0)>(vb), h0 = tr_read<v_rd_off(D0, 0, 1)>(vb), l1 = tr_read<v_rd_off(D0, 1, 0)>(vb), h1 = tr_read<v_rd_off(D0, 1, 1)>(vb);
;     const s16x4 l2 = tr_read<v_rd_off(D0, 2, 0)>(vb), h2 = tr_read<v_rd_off(D0, 2, 1)>(vb), l3 = tr_read<v_rd_off(D0, 3, 0)>(vb), h3 = tr_read<v_rd_off(D0, 3, 1)>(vb);
;     asm volatile("s_waitcnt lgkmcnt(0)" ::: "memory"); AT_SBAR();
;     ...
;     od = __builtin_amdgcn_mfma_f32_32x32x16_bf16(AT_PK(l0, h0), pa0, od, 0, 0, 0);
;     od = __builtin_amdgcn_mfma_f32_32x32x16_bf16(AT_PK(l1, h1), pa1, od, 0, 0, 0);
;     od = __builtin_amdgcn_mfma_f32_32x32x16_bf16(AT_PK(l2, h2), pa2, od, 0, 0, 0);
;     od = __builtin_amdgcn_mfma_f32_32x32x16_bf16(AT_PK(l3, h3), pa3, od, 0, 0, 0);
; DI void attn_pass(const Frame& F, CvRide& cv, const bf16_t* __restrict__ Qb, const bf16_t* __restrict__ Kh, const bf16_t* __restrict__ Vh, char* lds, f32x16 (&o)[4], float& l_out, const int wave_s) {
;     ...
;     const unsigned cv_ldo = (unsigned)(((tid >> 4) * 2 * 2048 + (tid & 15) * 4) * 4), cv_sto = (unsigned)((tid >> 3) * 2048 + 8 * (tid & 7));
;     const int cv_lw = OFF_CV + (4 * (tid & 15)) * 68 + 2 * (tid >> 4), cv_lr = OFF_CV + (tid >> 3) * 68 + 8 * (tid & 7);
;     f32x4 cvA = f32x4{}, cvB = f32x4{}; unsigned cvr0 = 0, cvr1 = 0;
.LBB4_779:
	ds_read_b64_tr_b16 v[218:219], v182 offset:0x600
	ds_read_b64_tr_b16 v[220:221], v182 offset:0xe00
	ds_read_b64_tr_b16 v[222:223], v182 offset:0x1600
	ds_read_b64_tr_b16 v[224:225], v182 offset:0x1e00
	ds_read_b64_tr_b16 v[226:227], v182 offset:0x2600
	ds_read_b64_tr_b16 v[228:229], v182 offset:0x2e00
	ds_read_b64_tr_b16 v[230:231], v182 offset:0x3600
	ds_read_b64_tr_b16 v[232:233], v182 offset:0x3e00
	s_waitcnt lgkmcnt(0)
	s_nop 0
	v_mfma_f32_32x32x16_bf16 v[0:15], v[218:221], v[96:99], v[0:15]
	s_lshl_b32 s2, s15, 14
	s_add_i32 s2, s2, 0
	s_lshl_b32 s3, s15, 13
	v_add_u32_e32 v96, s2, v203
	s_sub_i32 s65, s2, s3
	s_waitcnt vmcnt(0)
	v_add_u32_e32 v97, s2, v204
	v_mfma_f32_32x32x16_bf16 v[0:15], v[222:225], v[108:111], v[0:15]
	ds_write_b128 v96, v[176:179]
	v_add_u32_e32 v96, s65, v205
	ds_write_b128 v97, v[172:175]
	ds_write_b128 v96, v[168:171] offset:49152
	s_andn2_b64 s[2:3], exec, s[22:23]
	s_andn2_b64 vcc, exec, s[22:23]
	v_mfma_f32_32x32x16_bf16 v[0:15], v[226:229], v[100:103], v[0:15]
	v_mfma_f32_32x32x16_bf16 v[0:15], v[230:233], v[104:107], v[0:15]
	s_cbranch_vccnz .LBB4_784
	v_med3_f32 v97, v160, -v255, v255
	v_med3_f32 v98, v164, -v255, v255
	v_cvt_scalef32_pk_fp8_f32 v99, v97, v98, s93
	v_med3_f32 v97, v161, -v255, v255
	v_med3_f32 v98, v165, -v255, v255
	v_cvt_scalef32_pk_fp8_f32 v100, v97, v98, s93
	v_med3_f32 v97, v162, -v255, v255
	v_med3_f32 v98, v166, -v255, v255
	s_bitcmp1_b32 s58, 0
	v_cvt_scalef32_pk_fp8_f32 v101, v97, v98, s93
	s_cselect_b32 s8, 0x1100, 0
	v_med3_f32 v97, v163, -v255, v255
	v_med3_f32 v98, v167, -v255, v255
	v_cmp_eq_u32_e32 vcc, 0, v181
	v_add_u32_e32 v96, s8, v195
	v_cvt_scalef32_pk_fp8_f32 v102, v97, v98, s93
	s_and_b64 vcc, exec, vcc
	s_and_b32 s22, s58, 31
	ds_write_b16 v96, v99
	ds_write_b16 v96, v100 offset:68
	ds_write_b16 v96, v101 offset:136
	ds_write_b16 v96, v102 offset:204
	s_cbranch_vccnz .LBB4_808
	s_lshl_b32 s8, s22, 7
	s_lshl_b32 s9, s58, 6
	s_and_b32 s8, s8, 0xf00
	s_and_b32 s9, s9, 64
	s_or_b32 s20, s8, s9
	s_cbranch_execnz .LBB4_783

; #define AT_SBAR() __builtin_amdgcn_sched_barrier(0)
; template <int OFF> DI s16x4 tr_read(int vb) { s16x4 r; asm volatile("ds_read_b64_tr_b16 %0, %1 offset:%2" : "=&v"(r) : "v"(vb), "i"(OFF) : "memory"); return r; }
; template <int D0> DI void pv_one(f32x16& od, int vb, bf16x8 pa0, bf16x8 pa1, bf16x8 pa2, bf16x8 pa3) {
;     const s16x4 l0 = tr_read<v_rd_off(D0, 0, 0)>(vb), h0 = tr_read<v_rd_off(D0, 0, 1)>(vb), l1 = tr_read<v_rd_off(D0, 1, 0)>(vb), h1 = tr_read<v_rd_off(D0, 1, 1)>(vb);
;     const s16x4 l2 = tr_read<v_rd_off(D0, 2, 0)>(vb), h2 = tr_read<v_rd_off(D0, 2, 1)>(vb), l3 = tr_read<v_rd_off(D0, 3, 0)>(vb), h3 = tr_read<v_rd_off(D0, 3, 1)>(vb);
;     asm volatile("s_waitcnt lgkmcnt(0)" ::: "memory"); AT_SBAR();
;     ...
;     od = __builtin_amdgcn_mfma_f32_32x32x16_bf16(AT_PK(l0, h0), pa0, od, 0, 0, 0);
;     od = __builtin_amdgcn_mfma_f32_32x32x16_bf16(AT_PK(l1, h1), pa1, od, 0, 0, 0);
;     od = __builtin_amdgcn_mfma_f32_32x32x16_bf16(AT_PK(l2, h2), pa2, od, 0, 0, 0);
;     od = __builtin_amdgcn_mfma_f32_32x32x16_bf16(AT_PK(l3, h3), pa3, od, 0, 0, 0);
; DI void attn_pass(const Frame& F, CvRide& cv, const bf16_t* __restrict__ Qb, const bf16_t* __restrict__ Kh, const bf16_t* __restrict__ Vh, char* lds, f32x16 (&o)[4], float& l_out, const int wave_s) {
;     ...
;     const unsigned cv_ldo = (unsigned)(((tid >> 4) * 2 * 2048 + (tid & 15) * 4) * 4), cv_sto = (unsigned)((tid >> 3) * 2048 + 8 * (tid & 7));
;     const int cv_lw = OFF_CV + (4 * (tid & 15)) * 68 + 2 * (tid >> 4), cv_lr = OFF_CV + (tid >> 3) * 68 + 8 * (tid & 7);
;     f32x4 cvA = f32x4{}, cvB = f32x4{}; unsigned cvr0 = 0, cvr1 = 0;
.LBB4_799:
	ds_read_b64_tr_b16 v[220:221], v219 offset:0x600
	ds_read_b64_tr_b16 v[222:223], v219 offset:0xe00
	ds_read_b64_tr_b16 v[224:225], v219 offset:0x1600
	ds_read_b64_tr_b16 v[226:227], v219 offset:0x1e00
	ds_read_b64_tr_b16 v[228:229], v219 offset:0x2600
	ds_read_b64_tr_b16 v[230:231], v219 offset:0x2e00
	ds_read_b64_tr_b16 v[232:233], v219 offset:0x3600
	ds_read_b64_tr_b16 v[234:235], v219 offset:0x3e00
	s_waitcnt lgkmcnt(0)
	s_nop 0
	v_mfma_f32_32x32x16_bf16 v[0:15], v[220:223], v[120:123], v[0:15]
	s_add_i32 s2, s31, 0
	v_add_u32_e32 v120, s2, v203
	s_waitcnt vmcnt(0)
	ds_write_b128 v120, v[176:179]
	s_mov_b32 s20, 0
	s_andn2_b64 vcc, exec, s[22:23]
	v_mfma_f32_32x32x16_bf16 v[0:15], v[224:227], v[124:127], v[0:15]
	v_mfma_f32_32x32x16_bf16 v[0:15], v[228:231], v[112:115], v[0:15]
	v_add_u32_e32 v112, s2, v204
	ds_write_b128 v112, v[172:175]
	v_lshl_add_u32 v112, s29, 13, v206
	ds_write_b128 v112, v[168:171] offset:49152
	s_andn2_b64 s[2:3], exec, s[22:23]
	v_mfma_f32_32x32x16_bf16 v[0:15], v[232:235], v[116:119], v[0:15]
	s_cbranch_vccnz .LBB4_804
	v_med3_f32 v113, v160, -v255, v255
	v_med3_f32 v114, v164, -v255, v255
	v_cvt_scalef32_pk_fp8_f32 v115, v113, v114, s93
	v_med3_f32 v113, v161, -v255, v255
	v_med3_f32 v114, v165, -v255, v255
	v_cvt_scalef32_pk_fp8_f32 v116, v113, v114, s93
	v_med3_f32 v113, v162, -v255, v255
	v_med3_f32 v114, v166, -v255, v255
	s_bitcmp1_b32 s58, 0
	v_cvt_scalef32_pk_fp8_f32 v117, v113, v114, s93
	s_cselect_b32 s8, 0x1100, 0
	v_med3_f32 v113, v163, -v255, v255
	v_med3_f32 v114, v167, -v255, v255
	v_cmp_eq_u32_e32 vcc, 0, v181
	v_add_u32_e32 v112, s8, v195
	v_cvt_scalef32_pk_fp8_f32 v118, v113, v114, s93
	s_and_b64 vcc, exec, vcc
	s_and_b32 s24, s58, 31
	ds_write_b16 v112, v115
	ds_write_b16 v112, v116 offset:68
	ds_write_b16 v112, v117 offset:136
	ds_write_b16 v112, v118 offset:204
	s_cbranch_vccnz .LBB4_809
	s_lshl_b32 s8, s24, 7
	s_lshl_b32 s9, s58, 6
	s_and_b32 s8, s8, 0xf00
	s_and_b32 s9, s9, 64
	s_or_b32 s20, s8, s9
	s_cbranch_execnz .LBB4_803

; DI int v_st(int k, int c) { const int kk = (k & ~0xC) | ((k & 4) << 1) | ((k & 8) >> 1); return ((kk >> 3) * 4 + (c >> 5)) * 512 + ((kk & 7) * 32 + (c & 31)) * 2; }
; DI void attn_pass(const Frame& F, CvRide& cv, const bf16_t* __restrict__ Qb, const bf16_t* __restrict__ Kh, const bf16_t* __restrict__ Vh, char* lds, f32x16 (&o)[4], float& l_out, const int wave_s) {
;     ...
;     float m_ref = 0.f, l_reg = 0.f; bf16x8 qr[4]; f32x16 negm = f32x16{};
; #pragma unroll
;     for (int d = 0; d < 4; ++d) o[d] = f32x16{};
;     const bf16_t* Qw = Qb + (size_t)(wid * 32 + r32) * 64 + hi * 8;
; #pragma unroll
;     for (int d0 = 0; d0 < 4; ++d0) qr[d0] = *reinterpret_cast<const bf16x8*>(Qw + d0 * 16);
;     const int sr = tid >> 4, sc = (tid & 15) * 8, vst0 = v_st(sr, sc), vst1 = v_st(32 + sr, sc);
;     const int kr = tid >> 3, kcb = (tid & 7) * 16, kst = AT_KSWZ(kr, kcb);
;     const int vb0 = (int)(uintptr_t)V_lds + v_rd_base(lane);
;     struct { bf16x8 vs0, vs1, ks0; } sr_[1];
;     const unsigned gvo = (unsigned)((sr * 128 + sc) * 2), gko = (unsigned)((kr * 64 + (tid & 7) * 8) * 2);
;     ...
;     const unsigned cv_ldo = (unsigned)(((tid >> 4) * 2 * 2048 + (tid & 15) * 4) * 4), cv_sto = (unsigned)((tid >> 3) * 2048 + 8 * (tid & 7));
;     const int cv_lw = OFF_CV + (4 * (tid & 15)) * 68 + 2 * (tid >> 4), cv_lr = OFF_CV + (tid >> 3) * 68 + 8 * (tid & 7);
;     f32x4 cvA = f32x4{}, cvB = f32x4{}; unsigned cvr0 = 0, cvr1 = 0;
;     ...
;     f32x16 pA0, pA1, pB0, pB1; float alA, alB; bf16x8 pa0, pa1, pa2, pa3; constexpr int NT = S / 64;
;     constexpr int SE = 0;
;     {
;         bf16x8 v10 = *reinterpret_cast<const bf16x8*>(&Vh[(size_t)(64 + sr) * 128 + sc]), v11 = *reinterpret_cast<const bf16x8*>(&Vh[(size_t)(96 + sr) * 128 + sc]);
;         bf16x8 k10 = *reinterpret_cast<const bf16x8*>(&Kh[(size_t)(64 + kr) * 64 + (tid & 7) * 8]);
;         AT_SLOAD(SE, 0); asm volatile("s_waitcnt vmcnt(0)" ::: "memory");
;         __syncthreads();
;         AT_SWRITE(0, SE);
;         *(bf16x8*)(V_lds + SHM_V + vst0) = v10; *(bf16x8*)(V_lds + SHM_V + vst1) = v11; *(bf16x8*)(K_lds + SHM_K + kst) = k10;
;         __syncthreads();
;     }
;     qkt(pA0, pA1, K_lds, qr, negm, r32, hi); partialSM(pA0, pA1, m_ref, negm, alA);
;     int s_prev = 0, s_cur = 1, s_next = 2;
.LBB4_838:
	v_lshlrev_b32_e32 v24, 4, v22
	v_lshlrev_b32_e32 v23, 3, v22
	v_and_b32_e32 v24, 0xc0, v24
	v_lshlrev_b32_e32 v22, 1, v22
	v_and_or_b32 v24, v23, 24, v24
	v_and_b32_e32 v22, 32, v22
	v_and_b32_e32 v23, 0x100, v23
	s_cmp_lg_u32 0, -1
	v_or3_b32 v198, v24, v22, v23
	s_cselect_b32 s2, 0, 0
	v_add_u32_e32 v191, s2, v198
	s_movk_i32 s2, 0x44
	v_lshl_or_b32 v209, v16, 14, v18
	v_mul_lo_u32 v16, v20, s2
	v_exp_f32_e32 v216, v0
	v_exp_f32_e32 v218, v1
	v_exp_f32_e32 v179, v2
	v_exp_f32_e32 v217, v3
	v_exp_f32_e32 v177, v4
	v_exp_f32_e32 v215, v5
	v_exp_f32_e32 v176, v6
	v_exp_f32_e32 v178, v7
	v_exp_f32_e32 v173, v8
	v_exp_f32_e32 v175, v9
	v_exp_f32_e32 v171, v10
	v_exp_f32_e32 v174, v11
	v_exp_f32_e32 v169, v12
	v_exp_f32_e32 v172, v13
	v_exp_f32_e32 v168, v14
	v_exp_f32_e32 v170, v15
	v_add_u32_e32 v0, 0, v21
	s_mov_b32 s2, 0x22000
	v_add3_u32 v189, v0, v16, s2
	v_add_u32_e32 v0, 0, v19
	v_mov_b32_e32 v162, v183
	v_mov_b32_e32 v163, v183
	v_mov_b32_e32 v32, v183
	v_mov_b32_e32 v33, v183
	v_mov_b32_e32 v46, v183
	v_mov_b32_e32 v47, v183
	v_lshl_or_b32 v188, v20, 11, v21
	v_add3_u32 v190, v0, v17, s2
	v_mov_b32_e32 v182, v183
	v_mov_b32_e32 v160, v183
	v_mov_b32_e32 v161, v183
	v_mov_b32_e32 v34, v183
	v_mov_b32_e32 v35, v183
	v_mov_b32_e32 v36, v183
	v_mov_b32_e32 v37, v183
	v_mov_b32_e32 v38, v183
	v_mov_b32_e32 v39, v183
	v_mov_b32_e32 v40, v183
	v_mov_b32_e32 v41, v183
	v_mov_b32_e32 v42, v183
	v_mov_b32_e32 v43, v183
	v_mov_b32_e32 v44, v183
	v_mov_b32_e32 v45, v183
	v_mov_b64_e32 v[62:63], v[46:47]
	v_mov_b64_e32 v[16:17], v[32:33]
	v_mov_b64_e32 v[0:1], v[32:33]
	v_mov_b64_e32 v[166:167], v[162:163]
	s_mov_b32 s23, 1
	s_mov_b32 s57, 2
	s_mov_b32 s56, 0xc3e00000
	v_mov_b32_e32 v210, 0x43e00000
	s_mov_b64 s[28:29], s[16:17]
	s_mov_b32 s26, 0
	v_mov_b64_e32 v[60:61], v[44:45]
	v_mov_b64_e32 v[58:59], v[42:43]
	v_mov_b64_e32 v[56:57], v[40:41]
	v_mov_b64_e32 v[54:55], v[38:39]
	v_mov_b64_e32 v[52:53], v[36:37]
	v_mov_b64_e32 v[50:51], v[34:35]
	v_mov_b64_e32 v[48:49], v[32:33]
	v_mov_b64_e32 v[18:19], v[34:35]
	v_mov_b64_e32 v[20:21], v[36:37]
	v_mov_b64_e32 v[22:23], v[38:39]
	v_mov_b64_e32 v[24:25], v[40:41]
	v_mov_b64_e32 v[26:27], v[42:43]
	v_mov_b64_e32 v[28:29], v[44:45]
	v_mov_b64_e32 v[30:31], v[46:47]
	v_mov_b64_e32 v[2:3], v[34:35]
	v_mov_b64_e32 v[4:5], v[36:37]
	v_mov_b64_e32 v[6:7], v[38:39]
	v_mov_b64_e32 v[8:9], v[40:41]
	v_mov_b64_e32 v[10:11], v[42:43]
	v_mov_b64_e32 v[12:13], v[44:45]
	v_mov_b64_e32 v[14:15], v[46:47]
	v_mov_b64_e32 v[164:165], v[160:161]
	s_mov_b32 s30, 0
	s_mov_b32 s63, 1
	v_mov_b64_e32 v[184:185], v[182:183]
	v_mov_b32_e32 v81, v80
	v_mov_b32_e32 v82, v80
	v_mov_b32_e32 v83, v80
	v_mov_b32_e32 v84, v80
	v_mov_b32_e32 v85, v80
	v_mov_b32_e32 v86, v80
	v_mov_b32_e32 v87, v80
	v_mov_b32_e32 v88, v80
	v_mov_b32_e32 v89, v80
	v_mov_b32_e32 v90, v80
	v_mov_b32_e32 v91, v80
	v_mov_b32_e32 v92, v80
	v_mov_b32_e32 v93, v80
	v_mov_b32_e32 v94, v80
	v_mov_b32_e32 v95, v80
	v_mov_b32_e32 v255, 0x3f600000
	s_mov_b32 s93, 0x3b000000

; #define AT_SBAR() __builtin_amdgcn_sched_barrier(0)
; template <int OFF> DI s16x4 tr_read(int vb) { s16x4 r; asm volatile("ds_read_b64_tr_b16 %0, %1 offset:%2" : "=&v"(r) : "v"(vb), "i"(OFF) : "memory"); return r; }
; template <int D0> DI void pv_one(f32x16& od, int vb, bf16x8 pa0, bf16x8 pa1, bf16x8 pa2, bf16x8 pa3) {
;     const s16x4 l0 = tr_read<v_rd_off(D0, 0, 0)>(vb), h0 = tr_read<v_rd_off(D0, 0, 1)>(vb), l1 = tr_read<v_rd_off(D0, 1, 0)>(vb), h1 = tr_read<v_rd_off(D0, 1, 1)>(vb);
;     const s16x4 l2 = tr_read<v_rd_off(D0, 2, 0)>(vb), h2 = tr_read<v_rd_off(D0, 2, 1)>(vb), l3 = tr_read<v_rd_off(D0, 3, 0)>(vb), h3 = tr_read<v_rd_off(D0, 3, 1)>(vb);
;     asm volatile("s_waitcnt lgkmcnt(0)" ::: "memory"); AT_SBAR();
;     ...
;     od = __builtin_amdgcn_mfma_f32_32x32x16_bf16(AT_PK(l0, h0), pa0, od, 0, 0, 0);
;     od = __builtin_amdgcn_mfma_f32_32x32x16_bf16(AT_PK(l1, h1), pa1, od, 0, 0, 0);
;     od = __builtin_amdgcn_mfma_f32_32x32x16_bf16(AT_PK(l2, h2), pa2, od, 0, 0, 0);
;     od = __builtin_amdgcn_mfma_f32_32x32x16_bf16(AT_PK(l3, h3), pa3, od, 0, 0, 0);
; DI void attn_pass(const Frame& F, CvRide& cv, const bf16_t* __restrict__ Qb, const bf16_t* __restrict__ Kh, const bf16_t* __restrict__ Vh, char* lds, f32x16 (&o)[4], float& l_out, const int wave_s) {
;     ...
;     const unsigned cv_ldo = (unsigned)(((tid >> 4) * 2 * 2048 + (tid & 15) * 4) * 4), cv_sto = (unsigned)((tid >> 3) * 2048 + 8 * (tid & 7));
;     const int cv_lw = OFF_CV + (4 * (tid & 15)) * 68 + 2 * (tid >> 4), cv_lr = OFF_CV + (tid >> 3) * 68 + 8 * (tid & 7);
;     f32x4 cvA = f32x4{}, cvB = f32x4{}; unsigned cvr0 = 0, cvr1 = 0;
.LBB4_853:
	ds_read_b64_tr_b16 v[214:215], v182 offset:0x600
	ds_read_b64_tr_b16 v[216:217], v182 offset:0xe00
	ds_read_b64_tr_b16 v[218:219], v182 offset:0x1600
	ds_read_b64_tr_b16 v[220:221], v182 offset:0x1e00
	ds_read_b64_tr_b16 v[222:223], v182 offset:0x2600
	ds_read_b64_tr_b16 v[224:225], v182 offset:0x2e00
	ds_read_b64_tr_b16 v[226:227], v182 offset:0x3600
	ds_read_b64_tr_b16 v[228:229], v182 offset:0x3e00
	s_waitcnt lgkmcnt(0)
	s_nop 0
	v_mfma_f32_32x32x16_bf16 v[0:15], v[214:217], v[96:99], v[0:15]
	s_lshl_b32 s2, s57, 14
	s_add_i32 s2, s2, 0
	s_lshl_b32 s3, s57, 13
	v_add_u32_e32 v96, s2, v199
	s_sub_i32 s76, s2, s3
	s_waitcnt vmcnt(0)
	v_add_u32_e32 v97, s2, v200
	v_mfma_f32_32x32x16_bf16 v[0:15], v[218:221], v[108:111], v[0:15]
	ds_write_b128 v96, v[176:179]
	v_add_u32_e32 v96, s76, v201
	ds_write_b128 v97, v[172:175]
	ds_write_b128 v96, v[168:171] offset:49152
	s_andn2_b64 s[2:3], exec, s[30:31]
	s_andn2_b64 vcc, exec, s[30:31]
	v_mfma_f32_32x32x16_bf16 v[0:15], v[222:225], v[100:103], v[0:15]
	v_mfma_f32_32x32x16_bf16 v[0:15], v[226:229], v[104:107], v[0:15]
	s_cbranch_vccnz .LBB4_858
	v_med3_f32 v97, v160, -v255, v255
	v_med3_f32 v98, v164, -v255, v255
	v_cvt_scalef32_pk_fp8_f32 v99, v97, v98, s93
	v_med3_f32 v97, v161, -v255, v255
	v_med3_f32 v98, v165, -v255, v255
	v_cvt_scalef32_pk_fp8_f32 v100, v97, v98, s93
	v_med3_f32 v97, v162, -v255, v255
	v_med3_f32 v98, v166, -v255, v255
	s_bitcmp1_b32 s58, 0
	v_cvt_scalef32_pk_fp8_f32 v101, v97, v98, s93
	s_cselect_b32 s8, 0x1100, 0
	v_med3_f32 v97, v163, -v255, v255
	v_med3_f32 v98, v167, -v255, v255
	v_cmp_eq_u32_e32 vcc, 0, v181
	v_add_u32_e32 v96, s8, v190
	v_cvt_scalef32_pk_fp8_f32 v102, v97, v98, s93
	s_and_b64 vcc, exec, vcc
	s_and_b32 s30, s58, 31
	ds_write_b16 v96, v99
	ds_write_b16 v96, v100 offset:68
	ds_write_b16 v96, v101 offset:136
	ds_write_b16 v96, v102 offset:204
	s_cbranch_vccnz .LBB4_882
	s_lshl_b32 s8, s30, 7
	s_lshl_b32 s9, s58, 6
	s_and_b32 s8, s8, 0xf00
	s_and_b32 s9, s9, 64
	s_or_b32 s26, s8, s9
	s_cbranch_execnz .LBB4_857

; #define AT_SBAR() __builtin_amdgcn_sched_barrier(0)
; template <int OFF> DI s16x4 tr_read(int vb) { s16x4 r; asm volatile("ds_read_b64_tr_b16 %0, %1 offset:%2" : "=&v"(r) : "v"(vb), "i"(OFF) : "memory"); return r; }
; template <int D0> DI void pv_one(f32x16& od, int vb, bf16x8 pa0, bf16x8 pa1, bf16x8 pa2, bf16x8 pa3) {
;     const s16x4 l0 = tr_read<v_rd_off(D0, 0, 0)>(vb), h0 = tr_read<v_rd_off(D0, 0, 1)>(vb), l1 = tr_read<v_rd_off(D0, 1, 0)>(vb), h1 = tr_read<v_rd_off(D0, 1, 1)>(vb);
;     const s16x4 l2 = tr_read<v_rd_off(D0, 2, 0)>(vb), h2 = tr_read<v_rd_off(D0, 2, 1)>(vb), l3 = tr_read<v_rd_off(D0, 3, 0)>(vb), h3 = tr_read<v_rd_off(D0, 3, 1)>(vb);
;     asm volatile("s_waitcnt lgkmcnt(0)" ::: "memory"); AT_SBAR();
;     ...
;     od = __builtin_amdgcn_mfma_f32_32x32x16_bf16(AT_PK(l0, h0), pa0, od, 0, 0, 0);
;     od = __builtin_amdgcn_mfma_f32_32x32x16_bf16(AT_PK(l1, h1), pa1, od, 0, 0, 0);
;     od = __builtin_amdgcn_mfma_f32_32x32x16_bf16(AT_PK(l2, h2), pa2, od, 0, 0, 0);
;     od = __builtin_amdgcn_mfma_f32_32x32x16_bf16(AT_PK(l3, h3), pa3, od, 0, 0, 0);
; DI void attn_pass(const Frame& F, CvRide& cv, const bf16_t* __restrict__ Qb, const bf16_t* __restrict__ Kh, const bf16_t* __restrict__ Vh, char* lds, f32x16 (&o)[4], float& l_out, const int wave_s) {
;     ...
;     const unsigned cv_ldo = (unsigned)(((tid >> 4) * 2 * 2048 + (tid & 15) * 4) * 4), cv_sto = (unsigned)((tid >> 3) * 2048 + 8 * (tid & 7));
;     const int cv_lw = OFF_CV + (4 * (tid & 15)) * 68 + 2 * (tid >> 4), cv_lr = OFF_CV + (tid >> 3) * 68 + 8 * (tid & 7);
;     f32x4 cvA = f32x4{}, cvB = f32x4{}; unsigned cvr0 = 0, cvr1 = 0;
.LBB4_873:
	ds_read_b64_tr_b16 v[216:217], v215 offset:0x600
	ds_read_b64_tr_b16 v[218:219], v215 offset:0xe00
	ds_read_b64_tr_b16 v[220:221], v215 offset:0x1600
	ds_read_b64_tr_b16 v[222:223], v215 offset:0x1e00
	ds_read_b64_tr_b16 v[224:225], v215 offset:0x2600
	ds_read_b64_tr_b16 v[226:227], v215 offset:0x2e00
	ds_read_b64_tr_b16 v[228:229], v215 offset:0x3600
	ds_read_b64_tr_b16 v[230:231], v215 offset:0x3e00
	s_waitcnt lgkmcnt(0)
	s_nop 0
	v_mfma_f32_32x32x16_bf16 v[0:15], v[216:219], v[120:123], v[0:15]
	s_add_i32 s2, s65, 0
	v_add_u32_e32 v120, s2, v199
	s_waitcnt vmcnt(0)
	ds_write_b128 v120, v[176:179]
	s_mov_b32 s26, 0
	s_andn2_b64 vcc, exec, s[30:31]
	v_mfma_f32_32x32x16_bf16 v[0:15], v[220:223], v[124:127], v[0:15]
	v_mfma_f32_32x32x16_bf16 v[0:15], v[224:227], v[112:115], v[0:15]
	v_add_u32_e32 v112, s2, v200
	ds_write_b128 v112, v[172:175]
	v_lshl_add_u32 v112, s63, 13, v202
	ds_write_b128 v112, v[168:171] offset:49152
	s_andn2_b64 s[2:3], exec, s[30:31]
	v_mfma_f32_32x32x16_bf16 v[0:15], v[228:231], v[116:119], v[0:15]
	s_cbranch_vccnz .LBB4_878
	v_med3_f32 v113, v160, -v255, v255
	v_med3_f32 v114, v164, -v255, v255
	v_cvt_scalef32_pk_fp8_f32 v115, v113, v114, s93
	v_med3_f32 v113, v161, -v255, v255
	v_med3_f32 v114, v165, -v255, v255
	v_cvt_scalef32_pk_fp8_f32 v116, v113, v114, s93
	v_med3_f32 v113, v162, -v255, v255
	v_med3_f32 v114, v166, -v255, v255
	s_bitcmp1_b32 s58, 0
	v_cvt_scalef32_pk_fp8_f32 v117, v113, v114, s93
	s_cselect_b32 s8, 0x1100, 0
	v_med3_f32 v113, v163, -v255, v255
	v_med3_f32 v114, v167, -v255, v255
	v_cmp_eq_u32_e32 vcc, 0, v181
	v_add_u32_e32 v112, s8, v190
	v_cvt_scalef32_pk_fp8_f32 v118, v113, v114, s93
	s_and_b64 vcc, exec, vcc
	s_and_b32 s34, s58, 31
	ds_write_b16 v112, v115
	ds_write_b16 v112, v116 offset:68
	ds_write_b16 v112, v117 offset:136
	ds_write_b16 v112, v118 offset:204
	s_cbranch_vccnz .LBB4_883
	s_lshl_b32 s8, s34, 7
	s_lshl_b32 s9, s58, 6
	s_and_b32 s8, s8, 0xf00
	s_and_b32 s9, s9, 64
	s_or_b32 s26, s8, s9
	s_cbranch_execnz .LBB4_877

; DI int v_st(int k, int c) { const int kk = (k & ~0xC) | ((k & 4) << 1) | ((k & 8) >> 1); return ((kk >> 3) * 4 + (c >> 5)) * 512 + ((kk & 7) * 32 + (c & 31)) * 2; }
; DI void attn_pass(const Frame& F, CvRide& cv, const bf16_t* __restrict__ Qb, const bf16_t* __restrict__ Kh, const bf16_t* __restrict__ Vh, char* lds, f32x16 (&o)[4], float& l_out, const int wave_s) {
;     ...
;     float m_ref = 0.f, l_reg = 0.f; bf16x8 qr[4]; f32x16 negm = f32x16{};
; #pragma unroll
;     for (int d = 0; d < 4; ++d) o[d] = f32x16{};
;     const bf16_t* Qw = Qb + (size_t)(wid * 32 + r32) * 64 + hi * 8;
; #pragma unroll
;     for (int d0 = 0; d0 < 4; ++d0) qr[d0] = *reinterpret_cast<const bf16x8*>(Qw + d0 * 16);
;     const int sr = tid >> 4, sc = (tid & 15) * 8, vst0 = v_st(sr, sc), vst1 = v_st(32 + sr, sc);
;     const int kr = tid >> 3, kcb = (tid & 7) * 16, kst = AT_KSWZ(kr, kcb);
;     const int vb0 = (int)(uintptr_t)V_lds + v_rd_base(lane);
;     struct { bf16x8 vs0, vs1, ks0; } sr_[1];
;     const unsigned gvo = (unsigned)((sr * 128 + sc) * 2), gko = (unsigned)((kr * 64 + (tid & 7) * 8) * 2);
;     ...
;     const unsigned cv_ldo = (unsigned)(((tid >> 4) * 2 * 2048 + (tid & 15) * 4) * 4), cv_sto = (unsigned)((tid >> 3) * 2048 + 8 * (tid & 7));
;     const int cv_lw = OFF_CV + (4 * (tid & 15)) * 68 + 2 * (tid >> 4), cv_lr = OFF_CV + (tid >> 3) * 68 + 8 * (tid & 7);
;     f32x4 cvA = f32x4{}, cvB = f32x4{}; unsigned cvr0 = 0, cvr1 = 0;
;     ...
;     f32x16 pA0, pA1, pB0, pB1; float alA, alB; bf16x8 pa0, pa1, pa2, pa3; constexpr int NT = S / 64;
;     constexpr int SE = 0;
;     {
;         bf16x8 v10 = *reinterpret_cast<const bf16x8*>(&Vh[(size_t)(64 + sr) * 128 + sc]), v11 = *reinterpret_cast<const bf16x8*>(&Vh[(size_t)(96 + sr) * 128 + sc]);
;         bf16x8 k10 = *reinterpret_cast<const bf16x8*>(&Kh[(size_t)(64 + kr) * 64 + (tid & 7) * 8]);
;         AT_SLOAD(SE, 0); asm volatile("s_waitcnt vmcnt(0)" ::: "memory");
;         __syncthreads();
;         AT_SWRITE(0, SE);
;         *(bf16x8*)(V_lds + SHM_V + vst0) = v10; *(bf16x8*)(V_lds + SHM_V + vst1) = v11; *(bf16x8*)(K_lds + SHM_K + kst) = k10;
;         __syncthreads();
;     }
;     qkt(pA0, pA1, K_lds, qr, negm, r32, hi); partialSM(pA0, pA1, m_ref, negm, alA);
;     int s_prev = 0, s_cur = 1, s_next = 2;
.LBB4_912:
	v_lshlrev_b32_e32 v24, 4, v22
	v_lshlrev_b32_e32 v23, 3, v22
	v_and_b32_e32 v24, 0xc0, v24
	v_lshlrev_b32_e32 v22, 1, v22
	v_and_or_b32 v24, v23, 24, v24
	v_and_b32_e32 v22, 32, v22
	v_and_b32_e32 v23, 0x100, v23
	s_cmp_lg_u32 0, -1
	v_or3_b32 v202, v24, v22, v23
	s_cselect_b32 s2, 0, 0
	v_add_u32_e32 v192, s2, v202
	s_movk_i32 s2, 0x44
	v_lshl_or_b32 v213, v16, 14, v18
	v_mul_lo_u32 v16, v20, s2
	v_exp_f32_e32 v220, v0
	v_add_u32_e32 v0, 0, v21
	s_mov_b32 s2, 0x22000
	v_add3_u32 v194, v0, v16, s2
	v_add_u32_e32 v0, 0, v19
	v_add3_u32 v195, v0, v17, s2
	s_and_b32 s2, s33, 7
	s_lshl_b32 s2, s2, 2
	s_lshl_b32 s3, s60, 1
	v_exp_f32_e32 v222, v1
	v_exp_f32_e32 v179, v2
	v_exp_f32_e32 v221, v3
	v_exp_f32_e32 v177, v4
	v_exp_f32_e32 v219, v5
	v_exp_f32_e32 v176, v6
	v_exp_f32_e32 v178, v7
	v_exp_f32_e32 v173, v8
	v_exp_f32_e32 v175, v9
	v_exp_f32_e32 v171, v10
	v_exp_f32_e32 v174, v11
	v_exp_f32_e32 v169, v12
	v_exp_f32_e32 v172, v13
	v_exp_f32_e32 v168, v14
	v_exp_f32_e32 v170, v15
	s_add_i32 s2, s2, s3
	s_add_i32 s2, s2, 32
	v_mov_b32_e32 v162, v183
	v_mov_b32_e32 v163, v183
	v_mov_b32_e32 v48, v183
	v_mov_b32_e32 v49, v183
	v_lshl_or_b32 v193, v20, 11, v21
	s_ashr_i32 s3, s2, 31
	v_mov_b32_e32 v182, v183
	v_mov_b32_e32 v160, v183
	v_mov_b32_e32 v161, v183
	v_mov_b32_e32 v50, v183
	v_mov_b32_e32 v51, v183
	v_mov_b32_e32 v52, v183
	v_mov_b32_e32 v53, v183
	v_mov_b32_e32 v54, v183
	v_mov_b32_e32 v55, v183
	v_mov_b32_e32 v56, v183
	v_mov_b32_e32 v57, v183
	v_mov_b32_e32 v58, v183
	v_mov_b32_e32 v59, v183
	v_mov_b32_e32 v60, v183
	v_mov_b32_e32 v61, v183
	v_mov_b32_e32 v62, v183
	v_mov_b32_e32 v63, v183
	v_mov_b64_e32 v[32:33], v[48:49]
	v_mov_b64_e32 v[16:17], v[48:49]
	v_mov_b64_e32 v[0:1], v[48:49]
	v_mov_b64_e32 v[166:167], v[162:163]
	s_mov_b32 s27, 1
	s_lshl_b64 s[20:21], s[2:3], 19
	s_mov_b32 s28, 0xc3e00000
	v_mov_b32_e32 v214, 0x43e00000
	s_mov_b32 s18, 0
	v_mov_b64_e32 v[34:35], v[50:51]
	v_mov_b64_e32 v[36:37], v[52:53]
	v_mov_b64_e32 v[38:39], v[54:55]
	v_mov_b64_e32 v[40:41], v[56:57]
	v_mov_b64_e32 v[42:43], v[58:59]
	v_mov_b64_e32 v[44:45], v[60:61]
	v_mov_b64_e32 v[46:47], v[62:63]
	v_mov_b64_e32 v[18:19], v[50:51]
	v_mov_b64_e32 v[20:21], v[52:53]
	v_mov_b64_e32 v[22:23], v[54:55]
	v_mov_b64_e32 v[24:25], v[56:57]
	v_mov_b64_e32 v[26:27], v[58:59]
	v_mov_b64_e32 v[28:29], v[60:61]
	v_mov_b64_e32 v[30:31], v[62:63]
	v_mov_b64_e32 v[2:3], v[50:51]
	v_mov_b64_e32 v[4:5], v[52:53]
	v_mov_b64_e32 v[6:7], v[54:55]
	v_mov_b64_e32 v[8:9], v[56:57]
	v_mov_b64_e32 v[10:11], v[58:59]
	v_mov_b64_e32 v[12:13], v[60:61]
	v_mov_b64_e32 v[14:15], v[62:63]
	v_mov_b64_e32 v[164:165], v[160:161]
	s_mov_b32 s22, 0
	s_mov_b32 s29, 1
	v_mov_b64_e32 v[184:185], v[182:183]
	v_mov_b32_e32 v81, v80
	v_mov_b32_e32 v82, v80
	v_mov_b32_e32 v83, v80
	v_mov_b32_e32 v84, v80
	v_mov_b32_e32 v85, v80
	v_mov_b32_e32 v86, v80
	v_mov_b32_e32 v87, v80
	v_mov_b32_e32 v88, v80
	v_mov_b32_e32 v89, v80
	v_mov_b32_e32 v90, v80
	v_mov_b32_e32 v91, v80
	v_mov_b32_e32 v92, v80
	v_mov_b32_e32 v93, v80
	v_mov_b32_e32 v94, v80
	v_mov_b32_e32 v95, v80
	v_mov_b32_e32 v255, 0x3f600000
	s_mov_b32 s93, 0x3b000000

; #define AT_SBAR() __builtin_amdgcn_sched_barrier(0)
; template <int OFF> DI s16x4 tr_read(int vb) { s16x4 r; asm volatile("ds_read_b64_tr_b16 %0, %1 offset:%2" : "=&v"(r) : "v"(vb), "i"(OFF) : "memory"); return r; }
; template <int D0> DI void pv_one(f32x16& od, int vb, bf16x8 pa0, bf16x8 pa1, bf16x8 pa2, bf16x8 pa3) {
;     const s16x4 l0 = tr_read<v_rd_off(D0, 0, 0)>(vb), h0 = tr_read<v_rd_off(D0, 0, 1)>(vb), l1 = tr_read<v_rd_off(D0, 1, 0)>(vb), h1 = tr_read<v_rd_off(D0, 1, 1)>(vb);
;     const s16x4 l2 = tr_read<v_rd_off(D0, 2, 0)>(vb), h2 = tr_read<v_rd_off(D0, 2, 1)>(vb), l3 = tr_read<v_rd_off(D0, 3, 0)>(vb), h3 = tr_read<v_rd_off(D0, 3, 1)>(vb);
;     asm volatile("s_waitcnt lgkmcnt(0)" ::: "memory"); AT_SBAR();
;     ...
;     od = __builtin_amdgcn_mfma_f32_32x32x16_bf16(AT_PK(l0, h0), pa0, od, 0, 0, 0);
;     od = __builtin_amdgcn_mfma_f32_32x32x16_bf16(AT_PK(l1, h1), pa1, od, 0, 0, 0);
;     od = __builtin_amdgcn_mfma_f32_32x32x16_bf16(AT_PK(l2, h2), pa2, od, 0, 0, 0);
;     od = __builtin_amdgcn_mfma_f32_32x32x16_bf16(AT_PK(l3, h3), pa3, od, 0, 0, 0);
.LBB4_927:
	ds_read_b64_tr_b16 v[218:219], v182 offset:0x600
	ds_read_b64_tr_b16 v[220:221], v182 offset:0xe00
	ds_read_b64_tr_b16 v[222:223], v182 offset:0x1600
	ds_read_b64_tr_b16 v[224:225], v182 offset:0x1e00
	ds_read_b64_tr_b16 v[226:227], v182 offset:0x2600
	ds_read_b64_tr_b16 v[228:229], v182 offset:0x2e00
	ds_read_b64_tr_b16 v[230:231], v182 offset:0x3600
	ds_read_b64_tr_b16 v[232:233], v182 offset:0x3e00
	s_waitcnt lgkmcnt(0)
	s_nop 0
	v_mfma_f32_32x32x16_bf16 v[0:15], v[218:221], v[96:99], v[0:15]
	s_lshl_b32 s2, s15, 14
	s_add_i32 s2, s2, 0
	s_lshl_b32 s3, s15, 13
	v_add_u32_e32 v96, s2, v203
	s_sub_i32 s54, s2, s3
	s_waitcnt vmcnt(0)
	v_add_u32_e32 v97, s2, v204
	v_mfma_f32_32x32x16_bf16 v[0:15], v[222:225], v[108:111], v[0:15]
	ds_write_b128 v96, v[176:179]
	v_add_u32_e32 v96, s54, v205
	ds_write_b128 v97, v[172:175]
	ds_write_b128 v96, v[168:171] offset:49152
	s_andn2_b64 s[2:3], exec, s[22:23]
	s_andn2_b64 vcc, exec, s[22:23]
	v_mfma_f32_32x32x16_bf16 v[0:15], v[226:229], v[100:103], v[0:15]
	v_mfma_f32_32x32x16_bf16 v[0:15], v[230:233], v[104:107], v[0:15]
	s_cbranch_vccnz .LBB4_932
	v_med3_f32 v97, v160, -v255, v255
	v_med3_f32 v98, v164, -v255, v255
	v_cvt_scalef32_pk_fp8_f32 v99, v97, v98, s93
	v_med3_f32 v97, v161, -v255, v255
	v_med3_f32 v98, v165, -v255, v255
	v_cvt_scalef32_pk_fp8_f32 v100, v97, v98, s93
	v_med3_f32 v97, v162, -v255, v255
	v_med3_f32 v98, v166, -v255, v255
	s_bitcmp1_b32 s58, 0
	v_cvt_scalef32_pk_fp8_f32 v101, v97, v98, s93
	s_cselect_b32 s8, 0x1100, 0
	v_med3_f32 v97, v163, -v255, v255
	v_med3_f32 v98, v167, -v255, v255
	v_cmp_eq_u32_e32 vcc, 0, v181
	v_add_u32_e32 v96, s8, v195
	v_cvt_scalef32_pk_fp8_f32 v102, v97, v98, s93
	s_and_b64 vcc, exec, vcc
	s_and_b32 s22, s58, 31
	ds_write_b16 v96, v99
	ds_write_b16 v96, v100 offset:68
	ds_write_b16 v96, v101 offset:136
	ds_write_b16 v96, v102 offset:204
	s_cbranch_vccnz .LBB4_956
	s_lshl_b32 s8, s22, 7
	s_lshl_b32 s9, s58, 6
	s_and_b32 s8, s8, 0xf00
	s_and_b32 s9, s9, 64
	s_or_b32 s18, s8, s9
	s_cbranch_execnz .LBB4_931

; #define AT_SBAR() __builtin_amdgcn_sched_barrier(0)
; template <int OFF> DI s16x4 tr_read(int vb) { s16x4 r; asm volatile("ds_read_b64_tr_b16 %0, %1 offset:%2" : "=&v"(r) : "v"(vb), "i"(OFF) : "memory"); return r; }
; template <int D0> DI void pv_one(f32x16& od, int vb, bf16x8 pa0, bf16x8 pa1, bf16x8 pa2, bf16x8 pa3) {
;     const s16x4 l0 = tr_read<v_rd_off(D0, 0, 0)>(vb), h0 = tr_read<v_rd_off(D0, 0, 1)>(vb), l1 = tr_read<v_rd_off(D0, 1, 0)>(vb), h1 = tr_read<v_rd_off(D0, 1, 1)>(vb);
;     const s16x4 l2 = tr_read<v_rd_off(D0, 2, 0)>(vb), h2 = tr_read<v_rd_off(D0, 2, 1)>(vb), l3 = tr_read<v_rd_off(D0, 3, 0)>(vb), h3 = tr_read<v_rd_off(D0, 3, 1)>(vb);
;     asm volatile("s_waitcnt lgkmcnt(0)" ::: "memory"); AT_SBAR();
;     ...
;     od = __builtin_amdgcn_mfma_f32_32x32x16_bf16(AT_PK(l0, h0), pa0, od, 0, 0, 0);
;     od = __builtin_amdgcn_mfma_f32_32x32x16_bf16(AT_PK(l1, h1), pa1, od, 0, 0, 0);
;     od = __builtin_amdgcn_mfma_f32_32x32x16_bf16(AT_PK(l2, h2), pa2, od, 0, 0, 0);
;     od = __builtin_amdgcn_mfma_f32_32x32x16_bf16(AT_PK(l3, h3), pa3, od, 0, 0, 0);
.LBB4_947:
	ds_read_b64_tr_b16 v[220:221], v219 offset:0x600
	ds_read_b64_tr_b16 v[222:223], v219 offset:0xe00
	ds_read_b64_tr_b16 v[224:225], v219 offset:0x1600
	ds_read_b64_tr_b16 v[226:227], v219 offset:0x1e00
	ds_read_b64_tr_b16 v[228:229], v219 offset:0x2600
	ds_read_b64_tr_b16 v[230:231], v219 offset:0x2e00
	ds_read_b64_tr_b16 v[232:233], v219 offset:0x3600
	ds_read_b64_tr_b16 v[234:235], v219 offset:0x3e00
	s_waitcnt lgkmcnt(0)
	s_nop 0
	v_mfma_f32_32x32x16_bf16 v[0:15], v[220:223], v[120:123], v[0:15]
	s_add_i32 s2, s31, 0
	v_add_u32_e32 v120, s2, v203
	s_waitcnt vmcnt(0)
	ds_write_b128 v120, v[176:179]
	s_mov_b32 s18, 0
	s_andn2_b64 vcc, exec, s[22:23]
	v_mfma_f32_32x32x16_bf16 v[0:15], v[224:227], v[124:127], v[0:15]
	v_mfma_f32_32x32x16_bf16 v[0:15], v[228:231], v[112:115], v[0:15]
	v_add_u32_e32 v112, s2, v204
	ds_write_b128 v112, v[172:175]
	v_lshl_add_u32 v112, s29, 13, v206
	ds_write_b128 v112, v[168:171] offset:49152
	s_andn2_b64 s[2:3], exec, s[22:23]
	v_mfma_f32_32x32x16_bf16 v[0:15], v[232:235], v[116:119], v[0:15]
	s_cbranch_vccnz .LBB4_952
	v_med3_f32 v113, v160, -v255, v255
	v_med3_f32 v114, v164, -v255, v255
	v_cvt_scalef32_pk_fp8_f32 v115, v113, v114, s93
	v_med3_f32 v113, v161, -v255, v255
	v_med3_f32 v114, v165, -v255, v255
	v_cvt_scalef32_pk_fp8_f32 v116, v113, v114, s93
	v_med3_f32 v113, v162, -v255, v255
	v_med3_f32 v114, v166, -v255, v255
	s_bitcmp1_b32 s58, 0
	v_cvt_scalef32_pk_fp8_f32 v117, v113, v114, s93
	s_cselect_b32 s8, 0x1100, 0
	v_med3_f32 v113, v163, -v255, v255
	v_med3_f32 v114, v167, -v255, v255
	v_cmp_eq_u32_e32 vcc, 0, v181
	v_add_u32_e32 v112, s8, v195
	v_cvt_scalef32_pk_fp8_f32 v118, v113, v114, s93
	s_and_b64 vcc, exec, vcc
	s_and_b32 s24, s58, 31
	ds_write_b16 v112, v115
	ds_write_b16 v112, v116 offset:68
	ds_write_b16 v112, v117 offset:136
	ds_write_b16 v112, v118 offset:204
	s_cbranch_vccnz .LBB4_957
	s_lshl_b32 s8, s24, 7
	s_lshl_b32 s9, s58, 6
	s_and_b32 s8, s8, 0xf00
	s_and_b32 s9, s9, 64
	s_or_b32 s18, s8, s9
	s_cbranch_execnz .LBB4_951
